# P7: expert bias (+1) folded into accumulator start values; next unit bias loaded during the epilogue; 128 epilogue adds and the bias wait removed
# speedup vs baseline: 1.0234x; 1.0075x over previous
.LBB0_783:
	v_and_b32_e32 v1, 48, v178
	v_lshlrev_b32_e32 v4, 2, v200
	v_lshl_or_b32 v2, s11, 6, v200
	v_lshl_or_b32 v3, v200, 6, v1
	s_lshl_b32 s11, s11, 13
	v_and_b32_e32 v4, 32, v4
	s_lshl_b32 s5, s5, 5
	v_bitop3_b32 v202, v3, s11, v4 bitop3:0xde
	s_and_b32 s5, s5, 0x60
	v_lshlrev_b32_e32 v3, 6, v178
	s_movk_i32 s11, 0x3c0
	v_and_or_b32 v1, v3, s11, v1
	s_lshl_b32 s11, s5, 7
	s_add_u32 s18, s6, 0x4000
	s_addc_u32 s19, s7, 0
	s_add_i32 s53, s46, 0x8000
	v_lshl_add_u64 v[4:5], s[18:19], 0, v[176:177]
	s_mov_b32 m0, s53
	s_add_i32 s54, s46, 0xa000
	s_waitcnt vmcnt(4)
	s_barrier
	global_load_lds_dwordx4 v[4:5], off
	v_lshl_add_u64 v[4:5], s[18:19], 0, v[180:181]
	s_add_u32 s18, s90, 0xd040080
	s_mov_b32 m0, s54
	s_addc_u32 s19, s91, 0
	global_load_lds_dwordx4 v[4:5], off
	s_add_i32 m0, s46, 0x18000
	v_lshl_add_u64 v[4:5], s[18:19], 0, v[182:183]
	global_load_lds_dwordx4 v[4:5], off
	s_add_i32 m0, s46, 0x1a000
	v_lshl_add_u64 v[4:5], s[18:19], 0, v[184:185]
	s_add_u32 s18, s6, 0x404000
	s_addc_u32 s19, s7, 0
	s_add_i32 s55, s46, 0xc000
	global_load_lds_dwordx4 v[4:5], off
	v_lshl_add_u64 v[4:5], s[18:19], 0, v[176:177]
	s_mov_b32 m0, s55
	s_add_i32 s56, s46, 0xe000
	global_load_lds_dwordx4 v[4:5], off
	v_lshl_add_u64 v[4:5], s[18:19], 0, v[180:181]
	s_mov_b32 m0, s56
	v_lshlrev_b32_e32 v3, 2, v178
	global_load_lds_dwordx4 v[4:5], off
	v_and_b32_e32 v3, 32, v3
	v_bitop3_b32 v6, s11, v1, v3 bitop3:0xf6
	v_mov_b32_e32 v1, v183
	v_lshl_add_u64 v[186:187], s[16:17], 0, v[0:1]
	s_ashr_i32 s17, s33, 31
	s_lshr_b32 s17, s17, 29
	s_add_i32 s17, s33, s17
	s_and_b32 s18, s17, -8
	s_ashr_i32 s16, s96, 3
	s_sub_i32 s18, s33, s18
	s_mul_i32 s16, s16, s18
	s_ashr_i32 s17, s17, 3
	s_add_i32 s18, s16, s17
	s_add_u32 s16, s90, s5
	s_addc_u32 s17, s91, 0
	s_and_b64 s[2:3], s[2:3], exec
	s_mov_b32 s2, 0x20944
	s_cselect_b32 s57, s18, s33
	s_add_i32 s58, s2, 0x100
	s_mov_b32 s2, 0x20948
	s_add_i32 s59, s2, 0x100
	s_mov_b32 s2, 0x2094c
	s_add_i32 s60, s2, 0x100
	s_mov_b32 s2, 0x20950
	s_add_i32 s61, s2, 0x100
	s_mov_b32 s2, 0x20954
	s_add_i32 s62, s2, 0x100
	s_mov_b32 s2, 0x20958
	s_add_i32 s63, s2, 0x100
	s_mov_b32 s2, 0x2095c
	s_add_i32 s64, s2, 0x100
	s_mov_b32 s2, 0x20960
	s_add_i32 s65, s2, 0x100
	s_mov_b32 s2, 0x20964
	s_add_i32 s68, s2, 0x100
	s_mov_b32 s2, 0x20968
	s_add_i32 s69, s2, 0x100
	s_mov_b32 s2, 0x2096c
	s_add_i32 s70, s2, 0x100
	s_mov_b32 s2, 0x20970
	s_addk_i32 s2, 0x100
	v_writelane_b32 v250, s2, 4
	s_mov_b32 s2, 0x20974
	s_addk_i32 s2, 0x100
	v_writelane_b32 v250, s2, 3
	s_mov_b32 s2, 0x20978
	s_addk_i32 s2, 0x100
	v_writelane_b32 v250, s2, 5
	s_mov_b32 s2, 0x2097c
	s_addk_i32 s2, 0x100
	v_writelane_b32 v250, s2, 6
	s_mov_b32 s2, 0x20980
	s_addk_i32 s2, 0x100
	v_writelane_b32 v250, s2, 7
	s_mov_b32 s2, 0x20984
	s_addk_i32 s2, 0x100
	v_writelane_b32 v250, s2, 8
	s_mov_b32 s2, 0x20988
	s_addk_i32 s2, 0x100
	v_writelane_b32 v250, s2, 9
	s_mov_b32 s2, 0x2098c
	s_addk_i32 s2, 0x100
	v_writelane_b32 v250, s2, 10
	s_mov_b32 s2, 0x20990
	s_addk_i32 s2, 0x100
	v_writelane_b32 v250, s2, 11
	s_mov_b32 s2, 0x20994
	s_addk_i32 s2, 0x100
	v_writelane_b32 v250, s2, 12
	s_mov_b32 s2, 0x20998
	s_addk_i32 s2, 0x100
	v_writelane_b32 v250, s2, 13
	s_mov_b32 s2, 0x2099c
	s_addk_i32 s2, 0x100
	v_writelane_b32 v250, s2, 14
	s_mov_b32 s2, 0x209a0
	s_addk_i32 s2, 0x100
	v_writelane_b32 v250, s2, 15
	s_mov_b32 s2, 0x209a4
	s_addk_i32 s2, 0x100
	v_writelane_b32 v250, s2, 16
	s_mov_b32 s2, 0x209a8
	s_addk_i32 s2, 0x100
	v_writelane_b32 v250, s2, 17
	s_mov_b32 s2, 0x209ac
	s_addk_i32 s2, 0x100
	v_writelane_b32 v250, s2, 18
	s_mov_b32 s2, 0x209b0
	s_addk_i32 s2, 0x100
	v_writelane_b32 v250, s2, 19
	s_mov_b32 s2, 0x209b4
	s_addk_i32 s2, 0x100
	v_writelane_b32 v250, s2, 20
	s_mov_b32 s2, 0x209b8
	s_addk_i32 s2, 0x100
	v_and_b32_e32 v4, 12, v218
	v_mov_b32_e32 v5, v183
	v_mov_b32_e32 v3, v183
	v_writelane_b32 v250, s2, 21
	s_mov_b32 s2, 0x209bc
	s_waitcnt vmcnt(6)
	v_lshlrev_b64 v[2:3], 7, v[2:3]
	v_lshl_add_u64 v[0:1], s[16:17], 0, v[4:5]
	s_addk_i32 s2, 0x100
	s_mov_b32 s11, 0x18000
	v_lshl_add_u64 v[0:1], v[0:1], 0, v[2:3]
	s_mov_b64 s[16:17], 0xf1a0000
	v_writelane_b32 v250, s2, 22
	s_mov_b32 s2, 0x14000
	v_lshl_add_u64 v[188:189], v[0:1], 0, s[16:17]
	v_mov_b32_e32 v203, 0x7f7f7f7f
	v_mov_b32_e32 v204, 0x79797979
	s_add_i32 s79, s2, 0x100
	s_mov_b64 s[16:17], 0x80
	s_lshl_b32 s73, s5, 2
	v_lshlrev_b32_e32 v194, 2, v4
	s_mov_b32 s80, 0xc0c00000
	s_mov_b32 s81, 0xc3e00000
	v_add_u32_e32 v205, 0x100, v6
	s_add_i32 s77, s11, 0x100
	v_mov_b32_e32 v206, 0x41000000
	v_mov_b32_e32 v207, 0x43e00000
	s_lshl_b32 s99, s4, 14
	s_lshl_b32 s100, s10, 2
	s_add_u32 s99, s99, s100
	s_add_u32 s99, s99, s73
	s_add_u32 s100, s82, s99
	s_addc_u32 s101, s83, 0
	global_load_dwordx4 v[172:175], v194, s[100:101]
	global_load_dwordx4 v[168:171], v194, s[100:101] offset:64
	s_add_u32 s100, s100, 0x2000
	s_addc_u32 s101, s101, 0
	global_load_dwordx4 v[140:143], v194, s[100:101]
	global_load_dwordx4 v[136:139], v194, s[100:101] offset:64
	s_waitcnt vmcnt(0)
	v_add_f32_e32 v140, 1.0, v140
	v_add_f32_e32 v141, 1.0, v141
	v_add_f32_e32 v142, 1.0, v142
	v_add_f32_e32 v143, 1.0, v143
	v_add_f32_e32 v136, 1.0, v136
	v_add_f32_e32 v137, 1.0, v137
	v_add_f32_e32 v138, 1.0, v138
	v_add_f32_e32 v139, 1.0, v139
	v_mov_b32_e32 v164, v172
	v_mov_b32_e32 v165, v173
	v_mov_b32_e32 v166, v174
	v_mov_b32_e32 v167, v175
	v_mov_b32_e32 v160, v168
	v_mov_b32_e32 v161, v169
	v_mov_b32_e32 v162, v170
	v_mov_b32_e32 v163, v171
	v_mov_b32_e32 v156, v172
	v_mov_b32_e32 v157, v173
	v_mov_b32_e32 v158, v174
	v_mov_b32_e32 v159, v175
	v_mov_b32_e32 v152, v168
	v_mov_b32_e32 v153, v169
	v_mov_b32_e32 v154, v170
	v_mov_b32_e32 v155, v171
	v_mov_b32_e32 v148, v172
	v_mov_b32_e32 v149, v173
	v_mov_b32_e32 v150, v174
	v_mov_b32_e32 v151, v175
	v_mov_b32_e32 v144, v168
	v_mov_b32_e32 v145, v169
	v_mov_b32_e32 v146, v170
	v_mov_b32_e32 v147, v171
	v_mov_b32_e32 v132, v140
	v_mov_b32_e32 v133, v141
	v_mov_b32_e32 v134, v142
	v_mov_b32_e32 v135, v143
	v_mov_b32_e32 v128, v136
	v_mov_b32_e32 v129, v137
	v_mov_b32_e32 v130, v138
	v_mov_b32_e32 v131, v139
	v_mov_b32_e32 v124, v140
	v_mov_b32_e32 v125, v141
	v_mov_b32_e32 v126, v142
	v_mov_b32_e32 v127, v143
	v_mov_b32_e32 v120, v136
	v_mov_b32_e32 v121, v137
	v_mov_b32_e32 v122, v138
	v_mov_b32_e32 v123, v139
	v_mov_b32_e32 v116, v140
	v_mov_b32_e32 v117, v141
	v_mov_b32_e32 v118, v142
	v_mov_b32_e32 v119, v143
	v_mov_b32_e32 v112, v136
	v_mov_b32_e32 v113, v137
	v_mov_b32_e32 v114, v138
	v_mov_b32_e32 v115, v139
	v_mov_b32_e32 v108, v172
	v_mov_b32_e32 v109, v173
	v_mov_b32_e32 v110, v174
	v_mov_b32_e32 v111, v175
	v_mov_b32_e32 v104, v168
	v_mov_b32_e32 v105, v169
	v_mov_b32_e32 v106, v170
	v_mov_b32_e32 v107, v171
	v_mov_b32_e32 v100, v172
	v_mov_b32_e32 v101, v173
	v_mov_b32_e32 v102, v174
	v_mov_b32_e32 v103, v175
	v_mov_b32_e32 v96, v168
	v_mov_b32_e32 v97, v169
	v_mov_b32_e32 v98, v170
	v_mov_b32_e32 v99, v171
	v_mov_b32_e32 v92, v172
	v_mov_b32_e32 v93, v173
	v_mov_b32_e32 v94, v174
	v_mov_b32_e32 v95, v175
	v_mov_b32_e32 v88, v168
	v_mov_b32_e32 v89, v169
	v_mov_b32_e32 v90, v170
	v_mov_b32_e32 v91, v171
	v_mov_b32_e32 v84, v172
	v_mov_b32_e32 v85, v173
	v_mov_b32_e32 v86, v174
	v_mov_b32_e32 v87, v175
	v_mov_b32_e32 v80, v168
	v_mov_b32_e32 v81, v169
	v_mov_b32_e32 v82, v170
	v_mov_b32_e32 v83, v171
	v_mov_b32_e32 v76, v140
	v_mov_b32_e32 v77, v141
	v_mov_b32_e32 v78, v142
	v_mov_b32_e32 v79, v143
	v_mov_b32_e32 v72, v136
	v_mov_b32_e32 v73, v137
	v_mov_b32_e32 v74, v138
	v_mov_b32_e32 v75, v139
	v_mov_b32_e32 v68, v140
	v_mov_b32_e32 v69, v141
	v_mov_b32_e32 v70, v142
	v_mov_b32_e32 v71, v143
	v_mov_b32_e32 v64, v136
	v_mov_b32_e32 v65, v137
	v_mov_b32_e32 v66, v138
	v_mov_b32_e32 v67, v139
	v_mov_b32_e32 v60, v140
	v_mov_b32_e32 v61, v141
	v_mov_b32_e32 v62, v142
	v_mov_b32_e32 v63, v143
	v_mov_b32_e32 v56, v136
	v_mov_b32_e32 v57, v137
	v_mov_b32_e32 v58, v138
	v_mov_b32_e32 v59, v139
	v_mov_b32_e32 v52, v140
	v_mov_b32_e32 v53, v141
	v_mov_b32_e32 v54, v142
	v_mov_b32_e32 v55, v143
	v_mov_b32_e32 v48, v136
	v_mov_b32_e32 v49, v137
	v_mov_b32_e32 v50, v138
	v_mov_b32_e32 v51, v139
	s_barrier
	s_branch .LBB0_785

.LBB0_827:
	s_ashr_i32 s5, s4, 31
	s_lshl_b64 s[26:27], s[4:5], 14
	s_add_u32 s5, s82, s26
	s_addc_u32 s23, s83, s27
	s_ashr_i32 s11, s10, 31
	s_lshl_b64 s[26:27], s[10:11], 2
	s_add_u32 s5, s5, s26
	s_addc_u32 s11, s23, s27
	s_add_u32 s26, s5, s73
	s_addc_u32 s27, s11, 0
	v_mov_b32_e32 v195, v183
	s_movk_i32 s5, 0x2000
	v_mov_b32_e32 v18, v183
	s_nop 0
	s_nop 0
	s_ashr_i32 s5, s45, 3
	s_ashr_i32 s11, s10, 7
	s_and_b32 s5, s5, -16
	s_add_i32 s26, s5, s11
	s_ashr_i32 s27, s26, 31
	s_lshl_b64 s[26:27], s[26:27], 14
	v_lshl_add_u64 v[16:17], v[188:189], 0, s[26:27]
	s_movk_i32 s5, 0x1000
	s_mov_b64 s[26:27], 0x40000
	v_bfe_u32 v251, v178, 4, 2
	v_mov_b32_e32 v255, 0
	v_mul_u32_u24_e32 v254, 0x7fc, v251
	v_lshl_add_u64 v[252:253], v[16:17], 0, v[254:255]
	v_lshl_add_u64 v[254:255], v[252:253], 0, s[26:27]
	v_min_f32_e32 v19, 0x40e00000, v172
	v_min_f32_e32 v20, 0x40e00000, v173
	v_mul_f32_e32 v27, 0xc01d265f, v19
	v_mul_f32_e32 v29, 0xc01d265f, v20
	v_exp_f32_e32 v27, v27
	v_exp_f32_e32 v29, v29
	v_min_f32_e32 v21, 0x40e00000, v174
	v_min_f32_e32 v22, 0x40e00000, v175
	v_mul_f32_e32 v31, 0xc01d265f, v21
	v_mul_f32_e32 v33, 0xc01d265f, v22
	v_min_f32_e32 v23, 0x40e00000, v168
	v_exp_f32_e32 v31, v31
	v_exp_f32_e32 v33, v33
	v_add_f32_e32 v27, 1.0, v27
	v_add_f32_e32 v29, 1.0, v29
	v_mul_f32_e32 v35, 0xc01d265f, v23
	v_rcp_f32_e32 v27, v27
	v_rcp_f32_e32 v29, v29
	v_exp_f32_e32 v35, v35
	v_med3_f32 v26, v140, s80, v206
	v_med3_f32 v28, v141, s80, v206
	v_add_f32_e32 v31, 1.0, v31
	v_add_f32_e32 v33, 1.0, v33
	v_rcp_f32_e32 v31, v31
	v_rcp_f32_e32 v33, v33
	v_mul_f32_e32 v19, v19, v27
	v_mul_f32_e32 v20, v20, v29
	v_min_f32_e32 v25, 0x40e00000, v170
	v_mul_f32_e32 v19, v26, v19
	v_mul_f32_e32 v20, v28, v20
	v_mul_f32_e32 v38, 0xc01d265f, v25
	v_add_f32_e32 v35, 1.0, v35
	v_med3_f32 v30, v142, s80, v206
	v_med3_f32 v32, v143, s80, v206
	v_rcp_f32_e32 v35, v35
	v_cvt_pk_fp8_f32 v18, v19, v20
	v_exp_f32_e32 v38, v38
	v_mul_f32_e32 v21, v21, v31
	v_mul_f32_e32 v22, v22, v33
	v_min_f32_e32 v24, 0x40e00000, v169
	v_mul_f32_e32 v21, v30, v21
	v_mul_f32_e32 v22, v32, v22
	v_mul_f32_e32 v37, 0xc01d265f, v24
	v_med3_f32 v34, v136, s80, v206
	v_mov_b32_e32 v20, v21
	v_mov_b32_e32 v21, v22
	v_mul_f32_e32 v23, v23, v35
	v_cvt_pk_fp8_f32 v18, v20, v21 op_sel:[0,0,1]
	v_min_f32_e32 v22, 0x40e00000, v171
	v_exp_f32_e32 v37, v37
	v_mul_f32_e32 v19, v34, v23
	v_add_f32_e32 v21, 1.0, v38
	v_mul_f32_e32 v23, 0xc01d265f, v22
	v_rcp_f32_e32 v21, v21
	v_exp_f32_e32 v23, v23
	v_mov_b32_e32 v236, v18
	v_add_f32_e32 v37, 1.0, v37
	v_med3_f32 v18, v138, s80, v206
	v_rcp_f32_e32 v37, v37
	v_mul_f32_e32 v21, v25, v21
	v_mul_f32_e32 v18, v18, v21
	v_add_f32_e32 v21, 1.0, v23
	v_rcp_f32_e32 v21, v21
	v_med3_f32 v36, v137, s80, v206
	v_mul_f32_e32 v24, v24, v37
	v_mul_f32_e32 v20, v36, v24
	v_mul_f32_e32 v21, v22, v21
	v_mov_b32_e32 v22, v183
	v_cvt_pk_fp8_f32 v22, v19, v20
	v_med3_f32 v19, v139, s80, v206
	s_lshl_b32 s99, s18, 14
	s_lshl_b32 s100, s19, 2
	s_add_u32 s99, s99, s100
	s_add_u32 s99, s99, s73
	s_add_u32 s100, s82, s99
	s_addc_u32 s101, s83, 0
	global_load_dwordx4 v[172:175], v194, s[100:101]
	global_load_dwordx4 v[168:171], v194, s[100:101] offset:64
	s_add_u32 s100, s100, 0x2000
	s_addc_u32 s101, s101, 0
	global_load_dwordx4 v[140:143], v194, s[100:101]
	global_load_dwordx4 v[136:139], v194, s[100:101] offset:64
	v_mul_f32_e32 v19, v19, v21
	v_cvt_pk_fp8_f32 v22, v18, v19 op_sel:[0,0,1]
	v_min_f32_e32 v18, 0x40e00000, v164
	v_mul_f32_e32 v19, 0xc01d265f, v18
	v_exp_f32_e32 v19, v19
	v_min_f32_e32 v21, 0x40e00000, v165
	v_mov_b32_e32 v240, v22
	v_add_f32_e32 v19, 1.0, v19
	v_mul_f32_e32 v22, 0xc01d265f, v21
	v_rcp_f32_e32 v19, v19
	v_exp_f32_e32 v22, v22
	v_mul_f32_e32 v18, v18, v19
	v_med3_f32 v19, v132, s80, v206
	v_mul_f32_e32 v18, v19, v18
	v_add_f32_e32 v19, 1.0, v22
	v_rcp_f32_e32 v19, v19
	v_med3_f32 v20, v133, s80, v206
	v_mul_f32_e32 v19, v21, v19
	v_mul_f32_e32 v19, v20, v19
	v_min_f32_e32 v20, 0x40e00000, v166
	v_mul_f32_e32 v21, 0xc01d265f, v20
	v_exp_f32_e32 v21, v21
	v_min_f32_e32 v23, 0x40e00000, v167
	v_mul_f32_e32 v24, 0xc01d265f, v23
	v_add_f32_e32 v21, 1.0, v21
	v_rcp_f32_e32 v21, v21
	v_exp_f32_e32 v24, v24
	v_mul_f32_e32 v20, v20, v21
	v_med3_f32 v21, v134, s80, v206
	v_mul_f32_e32 v20, v21, v20
	v_add_f32_e32 v21, 1.0, v24
	v_rcp_f32_e32 v21, v21
	s_nop 0
	v_mul_f32_e32 v21, v23, v21
	v_mov_b32_e32 v23, v183
	v_cvt_pk_fp8_f32 v23, v18, v19
	v_med3_f32 v18, v135, s80, v206
	v_mul_f32_e32 v18, v18, v21
	v_cvt_pk_fp8_f32 v23, v20, v18 op_sel:[0,0,1]
	v_min_f32_e32 v18, 0x40e00000, v160
	v_mul_f32_e32 v19, 0xc01d265f, v18
	v_exp_f32_e32 v19, v19
	v_min_f32_e32 v21, 0x40e00000, v161
	v_mul_f32_e32 v22, 0xc01d265f, v21
	v_add_f32_e32 v19, 1.0, v19
	v_rcp_f32_e32 v19, v19
	v_exp_f32_e32 v22, v22
	v_mul_f32_e32 v18, v18, v19
	v_med3_f32 v19, v128, s80, v206
	v_mul_f32_e32 v18, v19, v18
	v_add_f32_e32 v19, 1.0, v22
	v_rcp_f32_e32 v19, v19
	v_med3_f32 v20, v129, s80, v206
	v_mul_f32_e32 v19, v21, v19
	v_mul_f32_e32 v19, v20, v19
	v_min_f32_e32 v20, 0x40e00000, v162
	v_mul_f32_e32 v21, 0xc01d265f, v20
	v_exp_f32_e32 v21, v21
	v_mov_b32_e32 v237, v23
	v_min_f32_e32 v23, 0x40e00000, v163
	v_add_f32_e32 v21, 1.0, v21
	v_mul_f32_e32 v24, 0xc01d265f, v23
	v_rcp_f32_e32 v21, v21
	v_exp_f32_e32 v24, v24
	v_mul_f32_e32 v20, v20, v21
	v_med3_f32 v21, v130, s80, v206
	v_mul_f32_e32 v20, v21, v20
	v_add_f32_e32 v21, 1.0, v24
	v_rcp_f32_e32 v21, v21
	s_nop 0
	v_mul_f32_e32 v21, v23, v21
	v_mov_b32_e32 v23, v183
	v_cvt_pk_fp8_f32 v23, v18, v19
	v_med3_f32 v18, v131, s80, v206
	v_mul_f32_e32 v18, v18, v21
	v_cvt_pk_fp8_f32 v23, v20, v18 op_sel:[0,0,1]
	v_min_f32_e32 v18, 0x40e00000, v156
	v_mul_f32_e32 v19, 0xc01d265f, v18
	v_exp_f32_e32 v19, v19
	v_min_f32_e32 v21, 0x40e00000, v157
	v_mul_f32_e32 v22, 0xc01d265f, v21
	v_add_f32_e32 v19, 1.0, v19
	v_rcp_f32_e32 v19, v19
	v_exp_f32_e32 v22, v22
	v_mul_f32_e32 v18, v18, v19
	v_med3_f32 v19, v124, s80, v206
	v_mul_f32_e32 v18, v19, v18
	v_add_f32_e32 v19, 1.0, v22
	v_rcp_f32_e32 v19, v19
	v_med3_f32 v20, v125, s80, v206
	v_mul_f32_e32 v19, v21, v19
	v_mul_f32_e32 v19, v20, v19
	v_min_f32_e32 v20, 0x40e00000, v158
	v_mul_f32_e32 v21, 0xc01d265f, v20
	v_exp_f32_e32 v21, v21
	v_mov_b32_e32 v241, v23
	v_min_f32_e32 v23, 0x40e00000, v159
	v_add_f32_e32 v21, 1.0, v21
	v_mul_f32_e32 v24, 0xc01d265f, v23
	v_rcp_f32_e32 v21, v21
	v_exp_f32_e32 v24, v24
	v_mul_f32_e32 v20, v20, v21
	v_med3_f32 v21, v126, s80, v206
	v_mul_f32_e32 v20, v21, v20
	v_add_f32_e32 v21, 1.0, v24
	v_rcp_f32_e32 v21, v21
	s_nop 0
	v_mul_f32_e32 v21, v23, v21
	v_mov_b32_e32 v23, v183
	v_cvt_pk_fp8_f32 v23, v18, v19
	v_med3_f32 v18, v127, s80, v206
	v_mul_f32_e32 v18, v18, v21
	v_cvt_pk_fp8_f32 v23, v20, v18 op_sel:[0,0,1]
	v_min_f32_e32 v20, 0x40e00000, v152
	v_mul_f32_e32 v18, 0xc01d265f, v20
	v_exp_f32_e32 v21, v18
	v_min_f32_e32 v24, 0x40e00000, v153
	v_mul_f32_e32 v25, 0xc01d265f, v24
	v_add_f32_e32 v21, 1.0, v21
	v_rcp_f32_e32 v21, v21
	v_exp_f32_e32 v25, v25
	v_mul_f32_e32 v20, v20, v21
	v_med3_f32 v21, v120, s80, v206
	v_mul_f32_e32 v20, v21, v20
	v_add_f32_e32 v21, 1.0, v25
	v_rcp_f32_e32 v21, v21
	v_med3_f32 v22, v121, s80, v206
	v_mul_f32_e32 v21, v24, v21
	v_mul_f32_e32 v21, v22, v21
	v_min_f32_e32 v22, 0x40e00000, v154
	v_mul_f32_e32 v24, 0xc01d265f, v22
	v_exp_f32_e32 v24, v24
	v_min_f32_e32 v26, 0x40e00000, v155
	v_mul_f32_e32 v27, 0xc01d265f, v26
	v_add_f32_e32 v24, 1.0, v24
	v_rcp_f32_e32 v24, v24
	v_exp_f32_e32 v27, v27
	v_mul_f32_e32 v22, v22, v24
	v_med3_f32 v24, v122, s80, v206
	v_mul_f32_e32 v22, v24, v22
	v_add_f32_e32 v24, 1.0, v27
	v_rcp_f32_e32 v24, v24
	v_med3_f32 v25, v123, s80, v206
	v_mul_f32_e32 v24, v26, v24
	v_mul_f32_e32 v24, v25, v24
	v_mov_b32_e32 v25, v183
	v_cvt_pk_fp8_f32 v25, v20, v21
	v_min_f32_e32 v20, 0x40e00000, v148
	v_mul_f32_e32 v21, 0xc01d265f, v20
	v_exp_f32_e32 v21, v21
	v_cvt_pk_fp8_f32 v25, v22, v24 op_sel:[0,0,1]
	v_min_f32_e32 v24, 0x40e00000, v149
	v_add_f32_e32 v21, 1.0, v21
	v_mul_f32_e32 v26, 0xc01d265f, v24
	v_rcp_f32_e32 v21, v21
	v_exp_f32_e32 v26, v26
	v_mul_f32_e32 v20, v20, v21
	v_med3_f32 v21, v116, s80, v206
	v_mul_f32_e32 v20, v21, v20
	v_add_f32_e32 v21, 1.0, v26
	v_rcp_f32_e32 v21, v21
	v_med3_f32 v22, v117, s80, v206
	v_mul_f32_e32 v21, v24, v21
	v_mul_f32_e32 v21, v22, v21
	v_min_f32_e32 v22, 0x40e00000, v150
	v_mul_f32_e32 v24, 0xc01d265f, v22
	v_exp_f32_e32 v24, v24
	v_min_f32_e32 v27, 0x40e00000, v151
	v_mul_f32_e32 v28, 0xc01d265f, v27
	v_add_f32_e32 v24, 1.0, v24
	v_rcp_f32_e32 v24, v24
	v_exp_f32_e32 v28, v28
	v_mul_f32_e32 v22, v22, v24
	v_med3_f32 v24, v118, s80, v206
	v_mul_f32_e32 v22, v24, v22
	v_add_f32_e32 v24, 1.0, v28
	v_rcp_f32_e32 v24, v24
	v_med3_f32 v26, v119, s80, v206
	v_mul_f32_e32 v24, v27, v24
	v_mul_f32_e32 v24, v26, v24
	v_mov_b32_e32 v26, v183
	v_cvt_pk_fp8_f32 v26, v20, v21
	v_min_f32_e32 v20, 0x40e00000, v144
	v_mul_f32_e32 v21, 0xc01d265f, v20
	v_exp_f32_e32 v21, v21
	v_cvt_pk_fp8_f32 v26, v22, v24 op_sel:[0,0,1]
	v_min_f32_e32 v24, 0x40e00000, v145
	v_add_f32_e32 v21, 1.0, v21
	v_mul_f32_e32 v27, 0xc01d265f, v24
	v_rcp_f32_e32 v21, v21
	v_exp_f32_e32 v27, v27
	v_mul_f32_e32 v20, v20, v21
	v_med3_f32 v21, v112, s80, v206
	v_mul_f32_e32 v20, v21, v20
	v_add_f32_e32 v21, 1.0, v27
	v_rcp_f32_e32 v21, v21
	v_med3_f32 v22, v113, s80, v206
	v_mul_f32_e32 v21, v24, v21
	v_mul_f32_e32 v21, v22, v21
	v_min_f32_e32 v22, 0x40e00000, v146
	v_mul_f32_e32 v24, 0xc01d265f, v22
	v_exp_f32_e32 v24, v24
	v_min_f32_e32 v28, 0x40e00000, v147
	v_mul_f32_e32 v29, 0xc01d265f, v28
	v_add_f32_e32 v24, 1.0, v24
	v_rcp_f32_e32 v24, v24
	v_exp_f32_e32 v29, v29
	v_mul_f32_e32 v22, v22, v24
	v_med3_f32 v24, v114, s80, v206
	v_mul_f32_e32 v22, v24, v22
	v_add_f32_e32 v24, 1.0, v29
	v_rcp_f32_e32 v24, v24
	s_nop 0
	v_mul_f32_e32 v24, v28, v24
	v_mov_b32_e32 v28, v183
	v_cvt_pk_fp8_f32 v28, v20, v21
	v_med3_f32 v20, v115, s80, v206
	v_mul_f32_e32 v20, v20, v24
	v_add_co_u32_e32 v18, vcc, s5, v16
	v_addc_co_u32_e32 v19, vcc, 0, v17, vcc
	v_cvt_pk_fp8_f32 v28, v22, v20 op_sel:[0,0,1]
	v_mov_b32_e32 v238, v23
	v_mov_b32_e32 v242, v25
	v_mov_b32_e32 v239, v26
	v_mov_b32_e32 v243, v28
	s_nop 1
	v_permlane32_swap_b32_e32 v236, v238
	v_permlane32_swap_b32_e32 v237, v239
	v_permlane32_swap_b32_e32 v240, v242
	v_permlane32_swap_b32_e32 v241, v243
	s_nop 0
	v_permlane16_swap_b32_e32 v236, v237
	v_permlane16_swap_b32_e32 v238, v239
	v_permlane16_swap_b32_e32 v240, v241
	v_permlane16_swap_b32_e32 v242, v243
	global_store_dwordx4 v[252:253], v[236:239], off
	global_store_dwordx4 v[252:253], v[240:243], off offset:16
	v_min_f32_e32 v20, 0x40e00000, v108
	v_mul_f32_e32 v18, 0xc01d265f, v20
	v_exp_f32_e32 v21, v18
	v_min_f32_e32 v23, 0x40e00000, v109
	v_mul_f32_e32 v24, 0xc01d265f, v23
	v_add_f32_e32 v21, 1.0, v21
	v_rcp_f32_e32 v21, v21
	v_exp_f32_e32 v24, v24
	v_mul_f32_e32 v20, v20, v21
	v_med3_f32 v21, v76, s80, v206
	v_mul_f32_e32 v20, v21, v20
	v_add_f32_e32 v21, 1.0, v24
	v_rcp_f32_e32 v21, v21
	v_med3_f32 v22, v77, s80, v206
	v_mul_f32_e32 v21, v23, v21
	v_mul_f32_e32 v21, v22, v21
	v_min_f32_e32 v22, 0x40e00000, v110
	v_mul_f32_e32 v23, 0xc01d265f, v22
	v_exp_f32_e32 v23, v23
	v_min_f32_e32 v25, 0x40e00000, v111
	v_mul_f32_e32 v26, 0xc01d265f, v25
	v_add_f32_e32 v23, 1.0, v23
	v_rcp_f32_e32 v23, v23
	v_exp_f32_e32 v26, v26
	v_mul_f32_e32 v22, v22, v23
	v_med3_f32 v23, v78, s80, v206
	v_mul_f32_e32 v22, v23, v22
	v_add_f32_e32 v23, 1.0, v26
	v_rcp_f32_e32 v23, v23
	s_nop 0
	v_mul_f32_e32 v23, v25, v23
	v_mov_b32_e32 v25, v183
	v_cvt_pk_fp8_f32 v25, v20, v21
	v_med3_f32 v20, v79, s80, v206
	v_mul_f32_e32 v20, v20, v23
	v_cvt_pk_fp8_f32 v25, v22, v20 op_sel:[0,0,1]
	v_min_f32_e32 v20, 0x40e00000, v104
	v_mul_f32_e32 v21, 0xc01d265f, v20
	v_exp_f32_e32 v21, v21
	v_min_f32_e32 v23, 0x40e00000, v105
	v_mul_f32_e32 v24, 0xc01d265f, v23
	v_add_f32_e32 v21, 1.0, v21
	v_rcp_f32_e32 v21, v21
	v_exp_f32_e32 v24, v24
	v_mul_f32_e32 v20, v20, v21
	v_med3_f32 v21, v72, s80, v206
	v_mul_f32_e32 v20, v21, v20
	v_add_f32_e32 v21, 1.0, v24
	v_rcp_f32_e32 v21, v21
	v_med3_f32 v22, v73, s80, v206
	v_mul_f32_e32 v21, v23, v21
	v_mul_f32_e32 v21, v22, v21
	v_min_f32_e32 v22, 0x40e00000, v106
	v_mul_f32_e32 v23, 0xc01d265f, v22
	s_mov_b32 s5, 0x41000
	v_lshl_add_u64 v[18:19], v[16:17], 0, s[26:27]
	v_add_co_u32_e32 v16, vcc, s5, v16
	v_exp_f32_e32 v23, v23
	s_nop 0
	v_addc_co_u32_e32 v17, vcc, 0, v17, vcc
	v_mov_b32_e32 v244, v25
	v_min_f32_e32 v25, 0x40e00000, v107
	v_add_f32_e32 v23, 1.0, v23
	v_mul_f32_e32 v26, 0xc01d265f, v25
	v_rcp_f32_e32 v23, v23
	v_exp_f32_e32 v26, v26
	v_mul_f32_e32 v22, v22, v23
	v_med3_f32 v23, v74, s80, v206
	v_mul_f32_e32 v22, v23, v22
	v_add_f32_e32 v23, 1.0, v26
	v_rcp_f32_e32 v23, v23
	s_nop 0
	v_mul_f32_e32 v23, v25, v23
	v_mov_b32_e32 v25, v183
	v_cvt_pk_fp8_f32 v25, v20, v21
	v_med3_f32 v20, v75, s80, v206
	v_mul_f32_e32 v20, v20, v23
	v_cvt_pk_fp8_f32 v25, v22, v20 op_sel:[0,0,1]
	v_min_f32_e32 v20, 0x40e00000, v100
	v_mul_f32_e32 v21, 0xc01d265f, v20
	v_exp_f32_e32 v21, v21
	v_min_f32_e32 v23, 0x40e00000, v101
	v_mul_f32_e32 v24, 0xc01d265f, v23
	v_add_f32_e32 v21, 1.0, v21
	v_rcp_f32_e32 v21, v21
	v_exp_f32_e32 v24, v24
	v_mul_f32_e32 v20, v20, v21
	v_med3_f32 v21, v68, s80, v206
	v_mul_f32_e32 v20, v21, v20
	v_add_f32_e32 v21, 1.0, v24
	v_rcp_f32_e32 v21, v21
	v_med3_f32 v22, v69, s80, v206
	v_mul_f32_e32 v21, v23, v21
	v_mul_f32_e32 v21, v22, v21
	v_min_f32_e32 v22, 0x40e00000, v102
	v_mul_f32_e32 v23, 0xc01d265f, v22
	v_exp_f32_e32 v23, v23
	v_mov_b32_e32 v236, v25
	v_min_f32_e32 v25, 0x40e00000, v103
	v_add_f32_e32 v23, 1.0, v23
	v_mul_f32_e32 v26, 0xc01d265f, v25
	v_rcp_f32_e32 v23, v23
	v_exp_f32_e32 v26, v26
	v_mul_f32_e32 v22, v22, v23
	v_med3_f32 v23, v70, s80, v206
	v_mul_f32_e32 v22, v23, v22
	v_add_f32_e32 v23, 1.0, v26
	v_rcp_f32_e32 v23, v23
	s_nop 0
	v_mul_f32_e32 v23, v25, v23
	v_mov_b32_e32 v25, v183
	v_cvt_pk_fp8_f32 v25, v20, v21
	v_med3_f32 v20, v71, s80, v206
	v_mul_f32_e32 v20, v20, v23
	v_cvt_pk_fp8_f32 v25, v22, v20 op_sel:[0,0,1]
	v_min_f32_e32 v20, 0x40e00000, v96
	v_mul_f32_e32 v21, 0xc01d265f, v20
	v_exp_f32_e32 v21, v21
	v_min_f32_e32 v23, 0x40e00000, v97
	v_mul_f32_e32 v24, 0xc01d265f, v23
	v_add_f32_e32 v21, 1.0, v21
	v_rcp_f32_e32 v21, v21
	v_exp_f32_e32 v24, v24
	v_mul_f32_e32 v20, v20, v21
	v_med3_f32 v21, v64, s80, v206
	v_mul_f32_e32 v20, v21, v20
	v_add_f32_e32 v21, 1.0, v24
	v_rcp_f32_e32 v21, v21
	v_med3_f32 v22, v65, s80, v206
	v_mul_f32_e32 v21, v23, v21
	v_mul_f32_e32 v21, v22, v21
	v_min_f32_e32 v22, 0x40e00000, v98
	v_mul_f32_e32 v23, 0xc01d265f, v22
	v_exp_f32_e32 v23, v23
	v_mov_b32_e32 v245, v25
	v_min_f32_e32 v25, 0x40e00000, v99
	v_add_f32_e32 v23, 1.0, v23
	v_mul_f32_e32 v26, 0xc01d265f, v25
	v_rcp_f32_e32 v23, v23
	v_exp_f32_e32 v26, v26
	v_mul_f32_e32 v22, v22, v23
	v_med3_f32 v23, v66, s80, v206
	v_mul_f32_e32 v22, v23, v22
	v_add_f32_e32 v23, 1.0, v26
	v_rcp_f32_e32 v23, v23
	s_nop 0
	v_mul_f32_e32 v23, v25, v23
	v_mov_b32_e32 v25, v183
	v_cvt_pk_fp8_f32 v25, v20, v21
	v_med3_f32 v20, v67, s80, v206
	v_mul_f32_e32 v20, v20, v23
	v_cvt_pk_fp8_f32 v25, v22, v20 op_sel:[0,0,1]
	v_min_f32_e32 v20, 0x40e00000, v92
	v_mul_f32_e32 v21, 0xc01d265f, v20
	v_exp_f32_e32 v21, v21
	v_mov_b32_e32 v237, v25
	v_med3_f32 v18, v60, s80, v206
	v_add_f32_e32 v19, 1.0, v21
	v_min_f32_e32 v21, 0x40e00000, v93
	v_mul_f32_e32 v22, 0xc01d265f, v21
	v_rcp_f32_e32 v19, v19
	v_exp_f32_e32 v22, v22
	v_mul_f32_e32 v19, v20, v19
	v_mul_f32_e32 v18, v18, v19
	v_add_f32_e32 v19, 1.0, v22
	v_rcp_f32_e32 v19, v19
	v_med3_f32 v20, v61, s80, v206
	v_mul_f32_e32 v19, v21, v19
	v_mul_f32_e32 v19, v20, v19
	v_min_f32_e32 v20, 0x40e00000, v94
	v_mul_f32_e32 v21, 0xc01d265f, v20
	v_exp_f32_e32 v21, v21
	v_min_f32_e32 v23, 0x40e00000, v95
	v_mul_f32_e32 v24, 0xc01d265f, v23
	v_add_f32_e32 v21, 1.0, v21
	v_rcp_f32_e32 v21, v21
	v_exp_f32_e32 v24, v24
	v_mul_f32_e32 v20, v20, v21
	v_med3_f32 v21, v62, s80, v206
	v_mul_f32_e32 v20, v21, v20
	v_add_f32_e32 v21, 1.0, v24
	v_rcp_f32_e32 v21, v21
	s_nop 0
	v_mul_f32_e32 v21, v23, v21
	v_mov_b32_e32 v23, v183
	v_cvt_pk_fp8_f32 v23, v18, v19
	v_med3_f32 v18, v63, s80, v206
	v_mul_f32_e32 v18, v18, v21
	v_cvt_pk_fp8_f32 v23, v20, v18 op_sel:[0,0,1]
	v_min_f32_e32 v18, 0x40e00000, v88
	v_mul_f32_e32 v19, 0xc01d265f, v18
	v_exp_f32_e32 v19, v19
	v_min_f32_e32 v21, 0x40e00000, v89
	v_mul_f32_e32 v22, 0xc01d265f, v21
	v_add_f32_e32 v19, 1.0, v19
	v_rcp_f32_e32 v19, v19
	v_exp_f32_e32 v22, v22
	v_mul_f32_e32 v18, v18, v19
	v_med3_f32 v19, v56, s80, v206
	v_mul_f32_e32 v18, v19, v18
	v_add_f32_e32 v19, 1.0, v22
	v_rcp_f32_e32 v19, v19
	v_med3_f32 v20, v57, s80, v206
	v_mul_f32_e32 v19, v21, v19
	v_mul_f32_e32 v19, v20, v19
	v_min_f32_e32 v20, 0x40e00000, v90
	v_mul_f32_e32 v21, 0xc01d265f, v20
	v_exp_f32_e32 v21, v21
	v_mov_b32_e32 v246, v23
	v_min_f32_e32 v23, 0x40e00000, v91
	v_add_f32_e32 v21, 1.0, v21
	v_mul_f32_e32 v24, 0xc01d265f, v23
	v_rcp_f32_e32 v21, v21
	v_exp_f32_e32 v24, v24
	v_mul_f32_e32 v20, v20, v21
	v_med3_f32 v21, v58, s80, v206
	v_mul_f32_e32 v20, v21, v20
	v_add_f32_e32 v21, 1.0, v24
	v_rcp_f32_e32 v21, v21
	s_nop 0
	v_mul_f32_e32 v21, v23, v21
	v_mov_b32_e32 v23, v183
	v_cvt_pk_fp8_f32 v23, v18, v19
	v_med3_f32 v18, v59, s80, v206
	v_mul_f32_e32 v18, v18, v21
	v_min_f32_e32 v8, 0x40e00000, v84
	v_cvt_pk_fp8_f32 v23, v20, v18 op_sel:[0,0,1]
	v_mul_f32_e32 v18, 0xc01d265f, v8
	v_exp_f32_e32 v18, v18
	v_min_f32_e32 v9, 0x40e00000, v85
	v_mul_f32_e32 v19, 0xc01d265f, v9
	v_add_f32_e32 v18, 1.0, v18
	v_rcp_f32_e32 v18, v18
	v_exp_f32_e32 v19, v19
	v_med3_f32 v12, v52, s80, v206
	v_mul_f32_e32 v8, v8, v18
	v_mul_f32_e32 v8, v12, v8
	v_add_f32_e32 v12, 1.0, v19
	v_rcp_f32_e32 v12, v12
	s_nop 0
	v_mul_f32_e32 v9, v9, v12
	v_med3_f32 v12, v53, s80, v206
	v_min_f32_e32 v10, 0x40e00000, v86
	v_mul_f32_e32 v9, v12, v9
	v_mul_f32_e32 v12, 0xc01d265f, v10
	v_exp_f32_e32 v12, v12
	v_min_f32_e32 v11, 0x40e00000, v87
	v_add_f32_e32 v12, 1.0, v12
	v_mul_f32_e32 v14, 0xc01d265f, v11
	v_rcp_f32_e32 v12, v12
	v_exp_f32_e32 v14, v14
	v_mul_f32_e32 v10, v10, v12
	v_med3_f32 v12, v54, s80, v206
	v_mul_f32_e32 v10, v12, v10
	v_add_f32_e32 v12, 1.0, v14
	v_rcp_f32_e32 v12, v12
	s_nop 0
	v_mul_f32_e32 v11, v11, v12
	v_mov_b32_e32 v12, v183
	v_cvt_pk_fp8_f32 v12, v8, v9
	v_med3_f32 v8, v55, s80, v206
	v_mul_f32_e32 v8, v8, v11
	v_min_f32_e32 v4, 0x40e00000, v80
	v_cvt_pk_fp8_f32 v12, v10, v8 op_sel:[0,0,1]
	v_mul_f32_e32 v8, 0xc01d265f, v4
	v_exp_f32_e32 v8, v8
	v_min_f32_e32 v5, 0x40e00000, v81
	v_mul_f32_e32 v9, 0xc01d265f, v5
	v_add_f32_e32 v8, 1.0, v8
	v_rcp_f32_e32 v8, v8
	v_exp_f32_e32 v9, v9
	v_med3_f32 v0, v48, s80, v206
	v_mul_f32_e32 v4, v4, v8
	v_mul_f32_e32 v0, v0, v4
	v_add_f32_e32 v4, 1.0, v9
	v_rcp_f32_e32 v4, v4
	v_med3_f32 v1, v49, s80, v206
	v_mul_f32_e32 v4, v5, v4
	v_mul_f32_e32 v1, v1, v4
	v_min_f32_e32 v4, 0x40e00000, v82
	v_mul_f32_e32 v5, 0xc01d265f, v4
	v_exp_f32_e32 v5, v5
	v_min_f32_e32 v6, 0x40e00000, v83
	v_mul_f32_e32 v7, 0xc01d265f, v6
	v_add_f32_e32 v5, 1.0, v5
	v_rcp_f32_e32 v5, v5
	v_exp_f32_e32 v7, v7
	v_med3_f32 v2, v50, s80, v206
	v_mul_f32_e32 v4, v4, v5
	v_mul_f32_e32 v2, v2, v4
	v_add_f32_e32 v4, 1.0, v7
	v_rcp_f32_e32 v4, v4
	v_mov_b32_e32 v5, v183
	v_cvt_pk_fp8_f32 v5, v0, v1
	v_mul_f32_e32 v4, v6, v4
	v_med3_f32 v0, v51, s80, v206
	v_mul_f32_e32 v0, v0, v4
	v_cvt_pk_fp8_f32 v5, v2, v0 op_sel:[0,0,1]
	s_andn2_b64 vcc, exec, s[24:25]
	v_mov_b32_e32 v238, v23
	v_mov_b32_e32 v247, v12
	v_mov_b32_e32 v239, v5
	s_nop 1
	v_permlane32_swap_b32_e32 v244, v246
	v_permlane32_swap_b32_e32 v245, v247
	v_permlane32_swap_b32_e32 v236, v238
	v_permlane32_swap_b32_e32 v237, v239
	s_nop 0
	v_permlane16_swap_b32_e32 v244, v245
	v_permlane16_swap_b32_e32 v246, v247
	v_permlane16_swap_b32_e32 v236, v237
	v_permlane16_swap_b32_e32 v238, v239
	global_store_dwordx4 v[254:255], v[244:247], off
	global_store_dwordx4 v[254:255], v[236:239], off offset:16
	s_cbranch_vccnz .LBB0_784
	s_mov_b32 s71, s44
	s_mov_b32 s8, s22
	s_mov_b64 s[6:7], s[20:21]
	s_mov_b32 s4, s18
	s_mov_b32 s45, s72
	s_mov_b32 s10, s19
	s_mov_b32 s76, s52
	s_waitcnt vmcnt(4)
	v_add_f32_e32 v140, 1.0, v140
	v_add_f32_e32 v141, 1.0, v141
	v_add_f32_e32 v142, 1.0, v142
	v_add_f32_e32 v143, 1.0, v143
	v_add_f32_e32 v136, 1.0, v136
	v_add_f32_e32 v137, 1.0, v137
	v_add_f32_e32 v138, 1.0, v138
	v_add_f32_e32 v139, 1.0, v139
	v_mov_b32_e32 v164, v172
	v_mov_b32_e32 v165, v173
	v_mov_b32_e32 v166, v174
	v_mov_b32_e32 v167, v175
	v_mov_b32_e32 v160, v168
	v_mov_b32_e32 v161, v169
	v_mov_b32_e32 v162, v170
	v_mov_b32_e32 v163, v171
	v_mov_b32_e32 v156, v172
	v_mov_b32_e32 v157, v173
	v_mov_b32_e32 v158, v174
	v_mov_b32_e32 v159, v175
	v_mov_b32_e32 v152, v168
	v_mov_b32_e32 v153, v169
	v_mov_b32_e32 v154, v170
	v_mov_b32_e32 v155, v171
	v_mov_b32_e32 v148, v172
	v_mov_b32_e32 v149, v173
	v_mov_b32_e32 v150, v174
	v_mov_b32_e32 v151, v175
	v_mov_b32_e32 v144, v168
	v_mov_b32_e32 v145, v169
	v_mov_b32_e32 v146, v170
	v_mov_b32_e32 v147, v171
	v_mov_b32_e32 v132, v140
	v_mov_b32_e32 v133, v141
	v_mov_b32_e32 v134, v142
	v_mov_b32_e32 v135, v143
	v_mov_b32_e32 v128, v136
	v_mov_b32_e32 v129, v137
	v_mov_b32_e32 v130, v138
	v_mov_b32_e32 v131, v139
	v_mov_b32_e32 v124, v140
	v_mov_b32_e32 v125, v141
	v_mov_b32_e32 v126, v142
	v_mov_b32_e32 v127, v143
	v_mov_b32_e32 v120, v136
	v_mov_b32_e32 v121, v137
	v_mov_b32_e32 v122, v138
	v_mov_b32_e32 v123, v139
	v_mov_b32_e32 v116, v140
	v_mov_b32_e32 v117, v141
	v_mov_b32_e32 v118, v142
	v_mov_b32_e32 v119, v143
	v_mov_b32_e32 v112, v136
	v_mov_b32_e32 v113, v137
	v_mov_b32_e32 v114, v138
	v_mov_b32_e32 v115, v139
	v_mov_b32_e32 v108, v172
	v_mov_b32_e32 v109, v173
	v_mov_b32_e32 v110, v174
	v_mov_b32_e32 v111, v175
	v_mov_b32_e32 v104, v168
	v_mov_b32_e32 v105, v169
	v_mov_b32_e32 v106, v170
	v_mov_b32_e32 v107, v171
	v_mov_b32_e32 v100, v172
	v_mov_b32_e32 v101, v173
	v_mov_b32_e32 v102, v174
	v_mov_b32_e32 v103, v175
	v_mov_b32_e32 v96, v168
	v_mov_b32_e32 v97, v169
	v_mov_b32_e32 v98, v170
	v_mov_b32_e32 v99, v171
	v_mov_b32_e32 v92, v172
	v_mov_b32_e32 v93, v173
	v_mov_b32_e32 v94, v174
	v_mov_b32_e32 v95, v175
	v_mov_b32_e32 v88, v168
	v_mov_b32_e32 v89, v169
	v_mov_b32_e32 v90, v170
	v_mov_b32_e32 v91, v171
	v_mov_b32_e32 v84, v172
	v_mov_b32_e32 v85, v173
	v_mov_b32_e32 v86, v174
	v_mov_b32_e32 v87, v175
	v_mov_b32_e32 v80, v168
	v_mov_b32_e32 v81, v169
	v_mov_b32_e32 v82, v170
	v_mov_b32_e32 v83, v171
	v_mov_b32_e32 v76, v140
	v_mov_b32_e32 v77, v141
	v_mov_b32_e32 v78, v142
	v_mov_b32_e32 v79, v143
	v_mov_b32_e32 v72, v136
	v_mov_b32_e32 v73, v137
	v_mov_b32_e32 v74, v138
	v_mov_b32_e32 v75, v139
	v_mov_b32_e32 v68, v140
	v_mov_b32_e32 v69, v141
	v_mov_b32_e32 v70, v142
	v_mov_b32_e32 v71, v143
	v_mov_b32_e32 v64, v136
	v_mov_b32_e32 v65, v137
	v_mov_b32_e32 v66, v138
	v_mov_b32_e32 v67, v139
	v_mov_b32_e32 v60, v140
	v_mov_b32_e32 v61, v141
	v_mov_b32_e32 v62, v142
	v_mov_b32_e32 v63, v143
	v_mov_b32_e32 v56, v136
	v_mov_b32_e32 v57, v137
	v_mov_b32_e32 v58, v138
	v_mov_b32_e32 v59, v139
	v_mov_b32_e32 v52, v140
	v_mov_b32_e32 v53, v141
	v_mov_b32_e32 v54, v142
	v_mov_b32_e32 v55, v143
	v_mov_b32_e32 v48, v136
	v_mov_b32_e32 v49, v137
	v_mov_b32_e32 v50, v138
	v_mov_b32_e32 v51, v139
	s_branch .LBB0_784
